# speedup vs baseline: 1.0213x; 1.0109x over previous
_Z11attn_kernelPKDF16_S0_PDF16_:
	s_load_dwordx4 s[4:7], s[0:1], 0x0
	s_load_dwordx2 s[8:9], s[0:1], 0x10
	s_lshr_b32 s1, s2, 3
	s_lshr_b32 s10, s2, 7
	s_and_b32 s0, s2, 4
	s_and_b32 s1, s1, 8
	s_and_b32 s20, s2, 3
	s_lshl_b32 s30, s10, 4
	s_or_b32 s22, s1, s0
	s_or_b32 s0, s30, s20
	s_or_b32 s14, s0, s22
	s_or_b32 s0, s20, 16
	s_sub_i32 s0, s0, s30
	s_mov_b32 s15, 0
	s_or_b32 s0, s0, s22
	s_bfe_u32 s24, s2, 0x30003
	s_ashr_i32 s1, s0, 31
	s_lshl_b64 s[2:3], s[14:15], 18
	s_waitcnt lgkmcnt(0)
	s_add_u32 s2, s4, s2
	s_addc_u32 s3, s5, s3
	s_lshl_b64 s[0:1], s[0:1], 18
	s_add_u32 s11, s4, s0
	s_addc_u32 s12, s5, s1
	s_add_u32 s13, s6, s0
	v_readfirstlane_b32 s16, v0
	s_addc_u32 s18, s7, s1
	s_lshl_b32 s0, s24, 2
	s_lshr_b32 s1, s16, 7
	s_add_i32 s14, s1, s0
	s_lshr_b32 s23, s16, 6
	s_lshl_b64 s[0:1], s[14:15], 13
	s_add_u32 s0, s2, s0
	v_and_b32_e32 v189, 31, v0
	s_addc_u32 s1, s3, s1
	s_lshl_b32 s21, s23, 5
	v_and_or_b32 v1, s21, 32, v189
	v_lshlrev_b32_e32 v186, 4, v1
	v_mov_b32_e32 v187, 0
	s_lshl_b32 s14, s23, 9
	v_lshl_add_u64 v[2:3], s[0:1], 0, v[186:187]
	s_and_b32 s0, s16, 0x3fffffc0
	s_lshl_b64 s[16:17], s[14:15], 1
	v_and_b32_e32 v188, 63, v0
	s_add_u32 s2, s11, s16
	s_addc_u32 s3, s12, s17
	s_add_u32 s44, s2, 0x8000
	s_addc_u32 s45, s3, 0
	v_lshlrev_b32_e32 v186, 4, v188
	v_lshl_add_u64 v[44:45], s[2:3], 0, v[186:187]
	s_add_u32 s2, s13, s16
	s_addc_u32 s3, s18, s17
	s_add_u32 s46, s2, 0x6000
	s_addc_u32 s47, s3, 0
	s_lshl_b32 s25, s23, 10
	s_cmp_lg_u32 0, -1
	s_cselect_b32 s1, 0, 0
	v_bfe_u32 v46, v0, 5, 1
	s_add_i32 s25, s25, s1
	s_mov_b32 s1, m0
	s_mov_b32 m0, s25
	s_nop 0
	global_load_lds_dwordx4 v[44:45], off
	s_mov_b32 m0, s1
	v_lshl_add_u64 v[34:35], s[2:3], 0, v[186:187]
	s_add_i32 s26, s25, 0x6000
	v_lshlrev_b32_e32 v4, 10, v46
	s_mov_b32 s1, m0
	s_mov_b32 m0, s26
	s_nop 0
	global_load_lds_dwordx4 v[34:35], off
	s_mov_b32 m0, s1
	s_mov_b64 s[18:19], 0x2000
	v_mov_b32_e32 v5, v187
	v_lshl_add_u64 v[6:7], v[44:45], 0, s[18:19]
	s_add_i32 s1, s25, 0x2000
	s_mov_b32 s2, m0
	s_mov_b32 m0, s1
	s_nop 0
	global_load_lds_dwordx4 v[6:7], off
	s_mov_b32 m0, s2
	v_lshl_add_u64 v[2:3], v[2:3], 0, v[4:5]
	global_load_dwordx4 v[136:139], v[2:3], off
	global_load_dwordx4 v[128:131], v[2:3], off offset:2048
	s_movk_i32 s1, 0x1000
	v_add_co_u32_e32 v2, vcc, s1, v2
	v_lshlrev_b32_e32 v1, 4, v189
	s_nop 0
	v_addc_co_u32_e32 v3, vcc, 0, v3, vcc
	global_load_dwordx4 v[120:123], v[2:3], off
	global_load_dwordx4 v[112:115], v[2:3], off offset:2048
	v_add3_u32 v184, 0, v4, v1
	v_mov_b32_e32 v2, v187
	v_mov_b32_e32 v3, v187
	v_mov_b32_e32 v4, v187
	v_mov_b32_e32 v6, v187
	v_mov_b32_e32 v7, v187
	v_mov_b32_e32 v8, v187
	v_mov_b32_e32 v9, v187
	v_mov_b32_e32 v10, v187
	v_mov_b32_e32 v11, v187
	v_mov_b32_e32 v12, v187
	v_mov_b32_e32 v13, v187
	v_mov_b32_e32 v14, v187
	v_mov_b32_e32 v15, v187
	v_mov_b32_e32 v16, v187
	v_mov_b32_e32 v17, v187
	s_mov_b64 s[2:3], 0x4000
	v_lshl_add_u64 v[18:19], v[44:45], 0, s[2:3]
	s_add_i32 s1, s25, 0x4000
	s_mov_b32 s11, m0
	s_mov_b32 m0, s1
	s_nop 0
	global_load_lds_dwordx4 v[18:19], off
	s_mov_b32 m0, s11
	v_lshl_add_u64 v[18:19], v[34:35], 0, s[18:19]
	s_add_i32 s1, s25, 0x8000
	s_mov_b32 s11, m0
	s_mov_b32 m0, s1
	s_nop 0
	global_load_lds_dwordx4 v[18:19], off
	s_mov_b32 m0, s11
	s_waitcnt vmcnt(4) lgkmcnt(0)
	s_barrier
	ds_read_b128 v[36:39], v184
	ds_read_b128 v[40:43], v184 offset:512
	v_lshlrev_b32_e32 v190, 3, v0
	s_mov_b64 s[12:13], 0x6000
	s_or_b32 s14, s22, s20
	s_sub_i32 s14, s14, s30
	s_add_i32 s34, s14, 16
	s_lshl_b32 s0, s0, 2
	s_ashr_i32 s35, s34, 31
	s_lshl_b64 s[34:35], s[34:35], 18
	s_mov_b32 s27, -1
	ds_read_b128 v[48:51], v184 offset:2048
	ds_read_b128 v[52:55], v184 offset:2560
	ds_read_b128 v[56:59], v184 offset:4096
	ds_read_b128 v[60:63], v184 offset:4608
	ds_read_b128 v[64:67], v184 offset:6144
	ds_read_b128 v[68:71], v184 offset:6656
	s_waitcnt vmcnt(3) lgkmcnt(7)
	v_mfma_f32_32x32x16_f16 v[18:33], v[36:39], v[136:139], v[2:17]
	s_movk_i32 s28, 0x6000
	s_movk_i32 s31, 0x2000
	s_movk_i32 s29, 0x4000
	v_lshlrev_b32_e32 v191, 9, v46
	v_lshlrev_b32_e32 v182, 4, v46
	v_lshlrev_b32_e32 v180, 4, v188
	s_waitcnt lgkmcnt(6)
	v_mfma_f32_32x32x16_f16 v[2:17], v[40:43], v[136:139], v[2:17]
	s_waitcnt vmcnt(2) lgkmcnt(5)
	v_mfma_f32_32x32x16_f16 v[18:33], v[48:51], v[128:131], v[18:33]
	s_waitcnt lgkmcnt(4)
	v_mfma_f32_32x32x16_f16 v[2:17], v[52:55], v[128:131], v[2:17]
	s_waitcnt vmcnt(1) lgkmcnt(3)
	v_mfma_f32_32x32x16_f16 v[18:33], v[56:59], v[120:123], v[18:33]
	s_waitcnt lgkmcnt(2)
	v_mfma_f32_32x32x16_f16 v[2:17], v[60:63], v[120:123], v[2:17]
	s_waitcnt vmcnt(0) lgkmcnt(1)
	v_mfma_f32_32x32x16_f16 v[18:33], v[64:67], v[112:115], v[18:33]
	s_waitcnt lgkmcnt(0)
	v_mfma_f32_32x32x16_f16 v[2:17], v[68:71], v[112:115], v[2:17]
	s_nop 11
	v_max_f32_e32 v1, v19, v18
	v_max3_f32 v37, v20, v21, v3
	v_max3_f32 v1, v1, v2, v4
	v_max3_f32 v36, v37, v24, v25
	v_max3_f32 v1, v1, v5, v22
	v_max3_f32 v36, v36, v8, v9
	v_max3_f32 v1, v1, v23, v6
	v_max3_f32 v36, v36, v28, v29
	v_max3_f32 v1, v1, v7, v26
	v_max3_f32 v36, v36, v12, v13
	v_max3_f32 v1, v1, v27, v10
	v_max3_f32 v36, v36, v32, v33
	v_max3_f32 v1, v1, v11, v30
	v_max3_f32 v36, v36, v16, v17
	v_max3_f32 v1, v1, v31, v14
	v_max3_f32 v1, v1, v15, v36
	v_mov_b32_e32 v36, v1
	s_nop 1
	v_permlane32_swap_b32_e32 v1, v36
	v_max_f32_e32 v183, v36, v1
	v_lshlrev_b32_e32 v1, 1, v0
	v_sub_f32_e32 v36, v2, v183
	v_and_b32_e32 v1, 32, v1
	v_and_b32_e32 v2, 24, v190
	v_lshlrev_b32_e32 v0, 4, v0
	v_add3_u32 v1, 0, v1, v2
	v_and_b32_e32 v0, 0xc0, v0
	v_lshlrev_b32_e32 v2, 8, v46
	v_add3_u32 v181, v1, v2, v0
	v_xor_b32_e32 v0, 0x80000000, v183
	v_sub_f32_e32 v37, v3, v183
	v_sub_f32_e32 v38, v4, v183
	v_sub_f32_e32 v39, v5, v183
	v_sub_f32_e32 v40, v6, v183
	v_sub_f32_e32 v41, v7, v183
	v_sub_f32_e32 v42, v8, v183
	v_sub_f32_e32 v43, v9, v183
	v_sub_f32_e32 v47, v10, v183
	v_sub_f32_e32 v57, v11, v183
	v_sub_f32_e32 v58, v12, v183
	v_sub_f32_e32 v59, v13, v183
	v_sub_f32_e32 v60, v14, v183
	v_sub_f32_e32 v61, v15, v183
	v_mov_b32_e32 v1, v0
	v_mov_b32_e32 v2, v0
	v_mov_b32_e32 v3, v0
	v_mov_b32_e32 v4, v0
	v_mov_b32_e32 v5, v0
	v_mov_b32_e32 v6, v0
	v_mov_b32_e32 v7, v0
	v_mov_b32_e32 v8, v0
	v_mov_b32_e32 v9, v0
	v_mov_b32_e32 v10, v0
	v_mov_b32_e32 v11, v0
	v_mov_b32_e32 v12, v0
	v_mov_b32_e32 v13, v0
	v_mov_b32_e32 v14, v0
	v_mov_b32_e32 v15, v0
	s_waitcnt vmcnt(0) lgkmcnt(0)
	s_barrier
	v_sub_f32_e32 v62, v16, v183
	v_sub_f32_e32 v63, v17, v183
	v_lshl_add_u64 v[16:17], v[44:45], 0, s[12:13]
	s_mov_b32 s1, m0
	s_mov_b32 m0, s25
	s_nop 0
	global_load_lds_dwordx4 v[16:17], off
	s_mov_b32 m0, s1
	s_add_i32 s1, s25, 0xa000
	v_lshl_add_u64 v[16:17], v[34:35], 0, s[2:3]
	s_mov_b32 s11, m0
	s_mov_b32 m0, s1
	s_nop 0
	global_load_lds_dwordx4 v[16:17], off
	s_mov_b32 m0, s11
	ds_read_b128 v[172:175], v184 offset:8192
	ds_read_b128 v[168:171], v184 offset:8704
	ds_read_b128 v[164:167], v184 offset:10240
	ds_read_b128 v[160:163], v184 offset:10752
	ds_read_b128 v[156:159], v184 offset:12288
	ds_read_b128 v[152:155], v184 offset:12800
	ds_read_b128 v[148:151], v184 offset:14336
	ds_read_b128 v[144:147], v184 offset:14848
	s_add_i32 s11, s0, 0
	v_sub_f32_e32 v18, v18, v183
	v_sub_f32_e32 v19, v19, v183
	v_sub_f32_e32 v20, v20, v183
	v_sub_f32_e32 v21, v21, v183
	v_sub_f32_e32 v22, v22, v183
	v_sub_f32_e32 v23, v23, v183
	v_sub_f32_e32 v24, v24, v183
	v_sub_f32_e32 v25, v25, v183
	v_sub_f32_e32 v26, v26, v183
	v_sub_f32_e32 v27, v27, v183
	v_sub_f32_e32 v28, v28, v183
	v_sub_f32_e32 v29, v29, v183
	v_sub_f32_e32 v30, v30, v183
	v_sub_f32_e32 v31, v31, v183
	v_sub_f32_e32 v32, v32, v183
	v_sub_f32_e32 v33, v33, v183
	s_add_u32 s14, s16, s34
	v_exp_f32_e32 v64, v18
	v_exp_f32_e32 v65, v19
	v_exp_f32_e32 v48, v36
	v_exp_f32_e32 v49, v37
	v_exp_f32_e32 v66, v20
	v_exp_f32_e32 v50, v38
	v_exp_f32_e32 v67, v21
	v_exp_f32_e32 v51, v39
	v_exp_f32_e32 v68, v22
	v_exp_f32_e32 v52, v40
	v_exp_f32_e32 v69, v23
	v_exp_f32_e32 v53, v41
	v_exp_f32_e32 v70, v24
	v_exp_f32_e32 v54, v42
	v_exp_f32_e32 v71, v25
	v_exp_f32_e32 v55, v43
	v_exp_f32_e32 v72, v26
	v_exp_f32_e32 v56, v47
	v_exp_f32_e32 v73, v27
	v_exp_f32_e32 v57, v57
	v_exp_f32_e32 v74, v28
	v_exp_f32_e32 v58, v58
	v_exp_f32_e32 v75, v29
	v_exp_f32_e32 v59, v59
	v_exp_f32_e32 v76, v30
	v_exp_f32_e32 v60, v60
	v_exp_f32_e32 v77, v31
	v_exp_f32_e32 v61, v61
	v_exp_f32_e32 v78, v32
	v_exp_f32_e32 v62, v62
	v_exp_f32_e32 v79, v33
	v_exp_f32_e32 v63, v63
	s_addc_u32 s16, s17, s35
	v_cmp_gt_u32_e64 s[0:1], 32, v188
	s_mov_b32 s16, 0x41000000
	s_mov_b32 s36, 0x43800000
	s_mov_b64 s[4:5], 0x8000
	s_movk_i32 s14, 0x2000
	s_movk_i32 s19, 0x4000
	v_mov_b32_e32 v16, v187
	v_mov_b32_e32 v17, v187
	v_mov_b32_e32 v18, v187
	v_mov_b32_e32 v19, v187
	v_mov_b32_e32 v20, v187
	v_mov_b32_e32 v21, v187
	v_mov_b32_e32 v22, v187
	v_mov_b32_e32 v23, v187
	v_mov_b32_e32 v24, v187
	v_mov_b32_e32 v25, v187
	v_mov_b32_e32 v26, v187
	v_mov_b32_e32 v27, v187
	v_mov_b32_e32 v28, v187
	v_mov_b32_e32 v29, v187
	v_mov_b32_e32 v30, v187
	v_mov_b32_e32 v31, v187
	v_mov_b32_e32 v32, v187
	v_mov_b32_e32 v33, v187
	v_mov_b32_e32 v34, v187
	v_mov_b32_e32 v35, v187
	v_mov_b32_e32 v36, v187
	v_mov_b32_e32 v37, v187
	v_mov_b32_e32 v38, v187
	v_mov_b32_e32 v39, v187
	v_mov_b32_e32 v40, v187
	v_mov_b32_e32 v41, v187
	v_mov_b32_e32 v42, v187
	v_mov_b32_e32 v43, v187
	v_mov_b32_e32 v44, v187
	v_mov_b32_e32 v45, v187
	v_mov_b32_e32 v46, v187
	v_mov_b32_e32 v47, v187
	v_lshl_add_u32 v186, v189, 2, s11
	s_waitcnt vmcnt(2) lgkmcnt(0)
	s_barrier
